# P5 GLU epilogue: sigmoid-argument constant folded into the gate dequant (64 v_mul fewer per wave-unit), 1+e via fma with c so rcp yields sigmoid/c; dead fp8 dest inits dropped
# speedup vs baseline: 1.0201x; 1.0038x over previous
.LBB0_555:
	v_and_b32_e32 v6, 15, v4
	s_lshl_b32 s5, s5, 5
	v_lshlrev_b32_e32 v7, 7, v6
	s_and_b32 s5, s5, 0x60
	v_lshl_or_b32 v7, s22, 13, v7
	s_add_u32 s22, s44, 0x80
	v_or_b32_e32 v6, s5, v6
	s_waitcnt vmcnt(2)
	s_barrier
	s_addc_u32 s23, s45, 0
	s_add_i32 s55, s29, 0x18000
	s_mov_b32 m0, s55
	s_nop 0
	global_load_lds_dwordx4 v1, s[22:23] offset:0
	s_add_i32 s56, s29, 0x1a000
	s_mov_b32 m0, s56
	s_nop 0
	global_load_lds_dwordx4 v173, s[22:23] offset:0
	s_add_u32 s22, s18, 0x80
	s_addc_u32 s23, s19, 0
	s_add_i32 s57, s29, 0x8000
	s_mov_b32 m0, s57
	s_nop 0
	global_load_lds_dwordx4 v171, s[22:23] offset:0
	s_add_i32 s58, s29, 0xa000
	s_mov_b32 m0, s58
	s_nop 0
	global_load_lds_dwordx4 v174, s[22:23] offset:0
	s_add_u32 s24, s44, 0x20080
	s_addc_u32 s25, s45, 0
	s_add_i32 s59, s29, 0x1c000
	s_mov_b32 m0, s59
	s_nop 0
	global_load_lds_dwordx4 v1, s[24:25] offset:0
	s_add_i32 s60, s29, 0x1e000
	s_add_i32 s61, s29, 0xc000
	v_bfe_u32 v8, v4, 4, 2
	v_bfe_u32 v4, v4, 1, 3
	s_mov_b32 m0, s60
	s_nop 0
	global_load_lds_dwordx4 v173, s[24:25] offset:0
	s_add_u32 s24, s18, 0x380
	v_bitop3_b32 v5, v5, v4, 3 bitop3:0x6c
	v_bitop3_b32 v4, v8, v4, 4 bitop3:0x36
	s_addc_u32 s25, s19, 0
	v_lshlrev_b32_e32 v5, 4, v5
	v_lshlrev_b32_e32 v4, 4, v4
	v_lshlrev_b32_e32 v6, 7, v6
	s_cmpk_lt_u32 s4, 0x100
	v_and_b32_e32 v3, 0x1000, v3
	s_movk_i32 s4, 0x1f0
	v_or_b32_e32 v176, v6, v5
	v_or_b32_e32 v177, v6, v4
	s_waitcnt vmcnt(6)
	s_cselect_b64 s[26:27], -1, 0
	v_and_or_b32 v178, v2, s4, v3
	s_add_i32 s4, 0, 0x10000
	v_or_b32_e32 v9, v5, v7
	v_or_b32_e32 v7, v4, v7
	v_add_u32_e32 v179, s4, v176
	v_add_u32_e32 v180, s4, v177
	s_add_i32 s4, 0, 0x14000
	s_add_i32 s62, s29, 0xe000
	v_add_u32_e32 v181, s4, v176
	v_add_u32_e32 v182, s4, v177
	v_add_u32_e32 v183, 0, v9
	v_add_u32_e32 v184, 0, v7
	v_mov_b32_e32 v185, 0x7f7f7f7f
	s_movk_i32 s63, 0xffc0
	v_mov_b32_e32 v163, 0
	s_mov_b32 s96, 0xbf1d265f
	s_mov_b32 s98, 0xb99d265f
	s_mov_b32 s100, 0xc01d265f
	s_mov_b32 s30, 0x39000000
	s_mov_b32 s64, 0xc0c00000
	v_mov_b32_e32 v186, 0x41000000
	s_barrier
	s_branch .LBB0_558

.LBB0_566:
	s_lshl_b32 s35, s67, 10
	v_mov_b32_e32 v25, v0
	s_and_b32 s35, s35, 0x400
	s_add_i32 s35, s35, 0
	v_lshrrev_b32_e32 v26, 1, v25
	v_and_b32_e32 v162, 0x60, v26
	v_lshlrev_b32_e32 v3, 1, v25
	s_add_i32 s35, s35, 0x24cc0
	v_lshlrev_b32_e32 v2, 2, v162
	v_and_b32_e32 v3, 0x60, v3
	v_add3_u32 v14, s35, v2, v3
	ds_read_b128 v[2:5], v14
	ds_read_b128 v[6:9], v14 offset:512
	ds_read_b128 v[10:13], v14 offset:16
	v_ashrrev_i32_e32 v24, 2, v25
	s_lshl_b32 s35, s40, 10
	s_lshl_b32 s38, s38, 7
	s_waitcnt lgkmcnt(2)
	v_pk_mul_f32 v[16:17], v[4:5], s[100:101] op_sel_hi:[1,0]
	v_pk_mul_f32 v[18:19], v[2:3], s[100:101] op_sel_hi:[1,0]
	ds_read_b128 v[2:5], v14 offset:528
	s_waitcnt lgkmcnt(2)
	v_pk_add_f32 v[20:21], v[8:9], 1.0 op_sel_hi:[1,0]
	s_waitcnt lgkmcnt(1)
	v_pk_mul_f32 v[8:9], v[12:13], s[100:101] op_sel_hi:[1,0]
	v_pk_add_f32 v[22:23], v[6:7], 1.0 op_sel_hi:[1,0]
	v_and_b32_e32 v6, 16, v26
	s_waitcnt lgkmcnt(0)
	v_pk_add_f32 v[14:15], v[2:3], 1.0 op_sel_hi:[1,0]
	v_and_b32_e32 v2, 15, v25
	v_pk_add_f32 v[12:13], v[4:5], 1.0 op_sel_hi:[1,0]
	v_and_or_b32 v2, v24, s63, v2
	v_pk_fma_f32 v[4:5], v[158:159], s[98:99], v[18:19] op_sel_hi:[1,0,1]
	v_lshl_add_u32 v24, s37, 8, v2
	v_pk_fma_f32 v[2:3], v[160:161], s[98:99], v[16:17] op_sel_hi:[1,0,1]
	v_max_f32_e32 v4, 0xc1898193, v4
	v_max_f32_e32 v5, 0xc1898193, v5
	v_max_f32_e32 v30, 0xc1898193, v2
	v_max_f32_e32 v31, 0xc1898193, v3
	v_exp_f32_e32 v2, v4
	v_exp_f32_e32 v3, v5
	v_exp_f32_e32 v32, v30
	v_exp_f32_e32 v33, v31
	v_pk_fma_f32 v[2:3], v[2:3], s[96:97], s[96:97] op_sel_hi:[1,0,0]
	v_pk_fma_f32 v[28:29], v[154:155], s[30:31], v[22:23] op_sel_hi:[1,0,1]
	v_rcp_f32_e32 v2, v2
	v_rcp_f32_e32 v3, v3
	v_med3_f32 v28, v28, s64, v186
	v_med3_f32 v29, v29, s64, v186
	v_pk_fma_f32 v[32:33], v[32:33], s[96:97], s[96:97] op_sel_hi:[1,0,0]
	v_pk_mul_f32 v[4:5], v[4:5], v[28:29]
	v_rcp_f32_e32 v32, v32
	v_rcp_f32_e32 v33, v33
	v_pk_mul_f32 v[4:5], v[4:5], v[2:3]
	v_pk_fma_f32 v[26:27], v[156:157], s[30:31], v[20:21] op_sel_hi:[1,0,1]
	v_cvt_pk_fp8_f32 v2, v4, v5
	v_med3_f32 v26, v26, s64, v186
	v_med3_f32 v27, v27, s64, v186
	v_pk_mul_f32 v[4:5], v[30:31], v[26:27]
	v_pk_mul_f32 v[10:11], v[10:11], s[100:101] op_sel_hi:[1,0]
	v_pk_mul_f32 v[4:5], v[4:5], v[32:33]
	v_pk_fma_f32 v[26:27], v[150:151], s[98:99], v[10:11] op_sel_hi:[1,0,1]
	v_cvt_pk_fp8_f32 v2, v4, v5 op_sel:[0,0,1]
	v_pk_fma_f32 v[4:5], v[152:153], s[98:99], v[8:9] op_sel_hi:[1,0,1]
	v_max_f32_e32 v26, 0xc1898193, v26
	v_max_f32_e32 v4, 0xc1898193, v4
	v_max_f32_e32 v27, 0xc1898193, v27
	v_max_f32_e32 v5, 0xc1898193, v5
	v_pk_fma_f32 v[30:31], v[146:147], s[30:31], v[14:15] op_sel_hi:[1,0,1]
	v_exp_f32_e32 v32, v26
	v_exp_f32_e32 v146, v4
	v_exp_f32_e32 v147, v5
	v_exp_f32_e32 v33, v27
	v_med3_f32 v30, v30, s64, v186
	v_med3_f32 v31, v31, s64, v186
	v_pk_fma_f32 v[146:147], v[146:147], s[96:97], s[96:97] op_sel_hi:[1,0,0]
	v_pk_fma_f32 v[32:33], v[32:33], s[96:97], s[96:97] op_sel_hi:[1,0,0]
	v_pk_mul_f32 v[26:27], v[26:27], v[30:31]
	v_rcp_f32_e32 v32, v32
	v_rcp_f32_e32 v33, v33
	v_rcp_f32_e32 v146, v146
	v_rcp_f32_e32 v147, v147
	v_pk_mul_f32 v[26:27], v[26:27], v[32:33]
	v_pk_fma_f32 v[28:29], v[148:149], s[30:31], v[12:13] op_sel_hi:[1,0,1]
	v_cvt_pk_fp8_f32 v3, v26, v27
	v_med3_f32 v28, v28, s64, v186
	v_med3_f32 v29, v29, s64, v186
	v_pk_mul_f32 v[4:5], v[4:5], v[28:29]
	v_pk_fma_f32 v[26:27], v[142:143], s[98:99], v[18:19] op_sel_hi:[1,0,1]
	v_pk_mul_f32 v[4:5], v[4:5], v[146:147]
	v_max_f32_e32 v26, 0xc1898193, v26
	v_cvt_pk_fp8_f32 v3, v4, v5 op_sel:[0,0,1]
	v_pk_fma_f32 v[4:5], v[144:145], s[98:99], v[16:17] op_sel_hi:[1,0,1]
	v_max_f32_e32 v27, 0xc1898193, v27
	v_max_f32_e32 v32, 0xc1898193, v4
	v_max_f32_e32 v33, 0xc1898193, v5
	v_exp_f32_e32 v4, v26
	v_exp_f32_e32 v5, v27
	v_pk_fma_f32 v[30:31], v[138:139], s[30:31], v[22:23] op_sel_hi:[1,0,1]
	v_exp_f32_e32 v138, v32
	v_exp_f32_e32 v139, v33
	v_pk_fma_f32 v[4:5], v[4:5], s[96:97], s[96:97] op_sel_hi:[1,0,0]
	v_med3_f32 v30, v30, s64, v186
	v_rcp_f32_e32 v4, v4
	v_rcp_f32_e32 v5, v5
	v_med3_f32 v31, v31, s64, v186
	v_pk_fma_f32 v[138:139], v[138:139], s[96:97], s[96:97] op_sel_hi:[1,0,0]
	v_pk_mul_f32 v[26:27], v[26:27], v[30:31]
	v_rcp_f32_e32 v138, v138
	v_rcp_f32_e32 v139, v139
	v_pk_mul_f32 v[26:27], v[26:27], v[4:5]
	v_pk_fma_f32 v[28:29], v[140:141], s[30:31], v[20:21] op_sel_hi:[1,0,1]
	v_cvt_pk_fp8_f32 v4, v26, v27
	v_med3_f32 v28, v28, s64, v186
	v_med3_f32 v29, v29, s64, v186
	v_pk_mul_f32 v[26:27], v[32:33], v[28:29]
	v_pk_fma_f32 v[28:29], v[134:135], s[98:99], v[10:11] op_sel_hi:[1,0,1]
	v_pk_mul_f32 v[26:27], v[26:27], v[138:139]
	v_max_f32_e32 v28, 0xc1898193, v28
	v_cvt_pk_fp8_f32 v4, v26, v27 op_sel:[0,0,1]
	v_pk_fma_f32 v[26:27], v[136:137], s[98:99], v[8:9] op_sel_hi:[1,0,1]
	v_pk_fma_f32 v[32:33], v[130:131], s[30:31], v[14:15] op_sel_hi:[1,0,1]
	v_max_f32_e32 v26, 0xc1898193, v26
	v_max_f32_e32 v29, 0xc1898193, v29
	v_max_f32_e32 v27, 0xc1898193, v27
	v_pk_fma_f32 v[30:31], v[132:133], s[30:31], v[12:13] op_sel_hi:[1,0,1]
	v_exp_f32_e32 v130, v28
	v_exp_f32_e32 v132, v26
	v_exp_f32_e32 v133, v27
	v_exp_f32_e32 v131, v29
	v_med3_f32 v32, v32, s64, v186
	v_med3_f32 v33, v33, s64, v186
	v_pk_fma_f32 v[132:133], v[132:133], s[96:97], s[96:97] op_sel_hi:[1,0,0]
	v_pk_fma_f32 v[130:131], v[130:131], s[96:97], s[96:97] op_sel_hi:[1,0,0]
	v_pk_mul_f32 v[28:29], v[28:29], v[32:33]
	v_rcp_f32_e32 v130, v130
	v_rcp_f32_e32 v131, v131
	v_rcp_f32_e32 v132, v132
	v_rcp_f32_e32 v133, v133
	v_pk_mul_f32 v[28:29], v[28:29], v[130:131]
	v_med3_f32 v30, v30, s64, v186
	v_cvt_pk_fp8_f32 v5, v28, v29
	v_pk_fma_f32 v[28:29], v[126:127], s[98:99], v[18:19] op_sel_hi:[1,0,1]
	v_med3_f32 v31, v31, s64, v186
	v_max_f32_e32 v28, 0xc1898193, v28
	v_max_f32_e32 v29, 0xc1898193, v29
	v_pk_mul_f32 v[26:27], v[26:27], v[30:31]
	v_pk_fma_f32 v[32:33], v[122:123], s[30:31], v[22:23] op_sel_hi:[1,0,1]
	v_pk_mul_f32 v[26:27], v[26:27], v[132:133]
	v_exp_f32_e32 v122, v28
	v_exp_f32_e32 v123, v29
	v_cvt_pk_fp8_f32 v5, v26, v27 op_sel:[0,0,1]
	v_pk_fma_f32 v[26:27], v[128:129], s[98:99], v[16:17] op_sel_hi:[1,0,1]
	v_pk_fma_f32 v[30:31], v[124:125], s[30:31], v[20:21] op_sel_hi:[1,0,1]
	v_max_f32_e32 v26, 0xc1898193, v26
	v_max_f32_e32 v27, 0xc1898193, v27
	v_exp_f32_e32 v124, v26
	v_exp_f32_e32 v125, v27
	v_pk_fma_f32 v[122:123], v[122:123], s[96:97], s[96:97] op_sel_hi:[1,0,0]
	v_med3_f32 v32, v32, s64, v186
	v_rcp_f32_e32 v122, v122
	v_rcp_f32_e32 v123, v123
	v_med3_f32 v33, v33, s64, v186
	v_pk_fma_f32 v[124:125], v[124:125], s[96:97], s[96:97] op_sel_hi:[1,0,0]
	v_pk_mul_f32 v[28:29], v[28:29], v[32:33]
	v_rcp_f32_e32 v124, v124
	v_rcp_f32_e32 v125, v125
	v_pk_mul_f32 v[32:33], v[28:29], v[122:123]
	v_cvt_pk_fp8_f32 v28, v32, v33
	v_med3_f32 v30, v30, s64, v186
	v_med3_f32 v31, v31, s64, v186
	v_pk_mul_f32 v[26:27], v[26:27], v[30:31]
	v_pk_fma_f32 v[30:31], v[118:119], s[98:99], v[10:11] op_sel_hi:[1,0,1]
	v_pk_mul_f32 v[26:27], v[26:27], v[124:125]
	v_max_f32_e32 v30, 0xc1898193, v30
	v_cvt_pk_fp8_f32 v28, v26, v27 op_sel:[0,0,1]
	v_pk_fma_f32 v[26:27], v[120:121], s[98:99], v[8:9] op_sel_hi:[1,0,1]
	v_pk_fma_f32 v[32:33], v[116:117], s[30:31], v[12:13] op_sel_hi:[1,0,1]
	v_max_f32_e32 v26, 0xc1898193, v26
	v_max_f32_e32 v31, 0xc1898193, v31
	v_max_f32_e32 v27, 0xc1898193, v27
	v_exp_f32_e32 v116, v30
	v_exp_f32_e32 v118, v26
	v_exp_f32_e32 v119, v27
	v_exp_f32_e32 v117, v31
	v_pk_fma_f32 v[114:115], v[114:115], s[30:31], v[14:15] op_sel_hi:[1,0,1]
	v_med3_f32 v114, v114, s64, v186
	v_pk_fma_f32 v[116:117], v[116:117], s[96:97], s[96:97] op_sel_hi:[1,0,0]
	v_med3_f32 v115, v115, s64, v186
	v_rcp_f32_e32 v116, v116
	v_rcp_f32_e32 v117, v117
	v_pk_fma_f32 v[118:119], v[118:119], s[96:97], s[96:97] op_sel_hi:[1,0,0]
	v_pk_mul_f32 v[30:31], v[30:31], v[114:115]
	v_rcp_f32_e32 v118, v118
	v_rcp_f32_e32 v119, v119
	v_pk_mul_f32 v[30:31], v[30:31], v[116:117]
	v_med3_f32 v32, v32, s64, v186
	v_cvt_pk_fp8_f32 v29, v30, v31
	v_pk_fma_f32 v[30:31], v[110:111], s[98:99], v[18:19] op_sel_hi:[1,0,1]
	v_med3_f32 v33, v33, s64, v186
	v_max_f32_e32 v30, 0xc1898193, v30
	v_max_f32_e32 v31, 0xc1898193, v31
	v_pk_mul_f32 v[26:27], v[26:27], v[32:33]
	v_pk_fma_f32 v[32:33], v[108:109], s[30:31], v[20:21] op_sel_hi:[1,0,1]
	v_pk_mul_f32 v[26:27], v[26:27], v[118:119]
	v_exp_f32_e32 v108, v30
	v_exp_f32_e32 v109, v31
	v_cvt_pk_fp8_f32 v29, v26, v27 op_sel:[0,0,1]
	v_pk_fma_f32 v[26:27], v[112:113], s[98:99], v[16:17] op_sel_hi:[1,0,1]
	v_pk_fma_f32 v[106:107], v[106:107], s[30:31], v[22:23] op_sel_hi:[1,0,1]
	v_max_f32_e32 v26, 0xc1898193, v26
	v_max_f32_e32 v27, 0xc1898193, v27
	v_exp_f32_e32 v110, v26
	v_exp_f32_e32 v111, v27
	v_pk_fma_f32 v[108:109], v[108:109], s[96:97], s[96:97] op_sel_hi:[1,0,0]
	v_med3_f32 v106, v106, s64, v186
	v_rcp_f32_e32 v108, v108
	v_rcp_f32_e32 v109, v109
	v_med3_f32 v107, v107, s64, v186
	v_pk_fma_f32 v[110:111], v[110:111], s[96:97], s[96:97] op_sel_hi:[1,0,0]
	v_pk_mul_f32 v[30:31], v[30:31], v[106:107]
	v_rcp_f32_e32 v110, v110
	v_rcp_f32_e32 v111, v111
	v_pk_mul_f32 v[106:107], v[30:31], v[108:109]
	v_cvt_pk_fp8_f32 v30, v106, v107
	v_med3_f32 v32, v32, s64, v186
	v_med3_f32 v33, v33, s64, v186
	v_pk_mul_f32 v[26:27], v[26:27], v[32:33]
	v_pk_fma_f32 v[32:33], v[102:103], s[98:99], v[10:11] op_sel_hi:[1,0,1]
	v_pk_mul_f32 v[26:27], v[26:27], v[110:111]
	v_max_f32_e32 v32, 0xc1898193, v32
	v_cvt_pk_fp8_f32 v30, v26, v27 op_sel:[0,0,1]
	v_pk_fma_f32 v[26:27], v[104:105], s[98:99], v[8:9] op_sel_hi:[1,0,1]
	v_max_f32_e32 v33, 0xc1898193, v33
	v_max_f32_e32 v26, 0xc1898193, v26
	v_max_f32_e32 v27, 0xc1898193, v27
	v_exp_f32_e32 v102, v32
	v_exp_f32_e32 v104, v26
	v_exp_f32_e32 v105, v27
	v_exp_f32_e32 v103, v33
	v_pk_fma_f32 v[98:99], v[98:99], s[30:31], v[14:15] op_sel_hi:[1,0,1]
	v_med3_f32 v98, v98, s64, v186
	v_pk_fma_f32 v[102:103], v[102:103], s[96:97], s[96:97] op_sel_hi:[1,0,0]
	v_med3_f32 v99, v99, s64, v186
	v_rcp_f32_e32 v102, v102
	v_rcp_f32_e32 v103, v103
	v_pk_fma_f32 v[104:105], v[104:105], s[96:97], s[96:97] op_sel_hi:[1,0,0]
	v_pk_mul_f32 v[32:33], v[32:33], v[98:99]
	v_rcp_f32_e32 v104, v104
	v_rcp_f32_e32 v105, v105
	v_pk_mul_f32 v[32:33], v[32:33], v[102:103]
	v_pk_fma_f32 v[100:101], v[100:101], s[30:31], v[12:13] op_sel_hi:[1,0,1]
	v_cvt_pk_fp8_f32 v31, v32, v33
	v_med3_f32 v100, v100, s64, v186
	v_med3_f32 v101, v101, s64, v186
	v_pk_mul_f32 v[26:27], v[26:27], v[100:101]
	v_and_b32_e32 v25, 16, v25
	v_pk_mul_f32 v[26:27], v[26:27], v[104:105]
	s_sub_i32 s38, s38, s35
	v_cvt_pk_fp8_f32 v31, v26, v27 op_sel:[0,0,1]
	v_or_b32_e32 v26, v24, v25
	v_ashrrev_i32_e32 v27, 31, v26
	v_lshlrev_b64 v[26:27], 10, v[26:27]
	s_ashr_i32 s39, s38, 31
	v_lshl_add_u64 v[26:27], s[12:13], 0, v[26:27]
	v_lshl_add_u64 v[26:27], v[26:27], 0, s[38:39]
	v_mov_b32_e32 v7, v163
	v_lshl_add_u64 v[26:27], v[26:27], 0, v[162:163]
	v_permlane16_swap_b32_e32 v2, v4
	v_permlane16_swap_b32_e32 v3, v5
	v_lshl_add_u64 v[26:27], v[26:27], 0, v[6:7]
	global_store_dwordx4 v[26:27], v[2:5], off
	v_or_b32_e32 v26, 32, v25
	v_permlane16_swap_b32_e32 v28, v30
	v_or_b32_e32 v2, v24, v26
	v_ashrrev_i32_e32 v3, 31, v2
	v_lshlrev_b64 v[2:3], 10, v[2:3]
	v_lshl_add_u64 v[2:3], s[12:13], 0, v[2:3]
	v_lshl_add_u64 v[2:3], v[2:3], 0, s[38:39]
	v_lshl_add_u64 v[2:3], v[2:3], 0, v[162:163]
	v_permlane16_swap_b32_e32 v29, v31
	v_lshl_add_u64 v[2:3], v[2:3], 0, v[6:7]
	v_pk_fma_f32 v[4:5], v[94:95], s[98:99], v[18:19] op_sel_hi:[1,0,1]
	global_store_dwordx4 v[2:3], v[28:31], off
	v_pk_fma_f32 v[2:3], v[96:97], s[98:99], v[16:17] op_sel_hi:[1,0,1]
	v_max_f32_e32 v4, 0xc1898193, v4
	v_max_f32_e32 v5, 0xc1898193, v5
	v_max_f32_e32 v32, 0xc1898193, v2
	v_max_f32_e32 v33, 0xc1898193, v3
	v_exp_f32_e32 v2, v4
	v_exp_f32_e32 v3, v5
	v_pk_fma_f32 v[30:31], v[90:91], s[30:31], v[22:23] op_sel_hi:[1,0,1]
	v_exp_f32_e32 v90, v32
	v_exp_f32_e32 v91, v33
	v_pk_fma_f32 v[2:3], v[2:3], s[96:97], s[96:97] op_sel_hi:[1,0,0]
	v_med3_f32 v30, v30, s64, v186
	v_rcp_f32_e32 v2, v2
	v_rcp_f32_e32 v3, v3
	v_med3_f32 v31, v31, s64, v186
	v_pk_fma_f32 v[28:29], v[92:93], s[30:31], v[20:21] op_sel_hi:[1,0,1]
	v_pk_fma_f32 v[90:91], v[90:91], s[96:97], s[96:97] op_sel_hi:[1,0,0]
	v_pk_mul_f32 v[4:5], v[4:5], v[30:31]
	v_med3_f32 v28, v28, s64, v186
	v_rcp_f32_e32 v90, v90
	v_rcp_f32_e32 v91, v91
	v_pk_mul_f32 v[4:5], v[4:5], v[2:3]
	v_med3_f32 v29, v29, s64, v186
	v_cvt_pk_fp8_f32 v2, v4, v5
	v_pk_mul_f32 v[4:5], v[32:33], v[28:29]
	v_pk_fma_f32 v[28:29], v[86:87], s[98:99], v[10:11] op_sel_hi:[1,0,1]
	v_pk_mul_f32 v[4:5], v[4:5], v[90:91]
	v_max_f32_e32 v28, 0xc1898193, v28
	v_max_f32_e32 v29, 0xc1898193, v29
	v_pk_fma_f32 v[32:33], v[82:83], s[30:31], v[14:15] op_sel_hi:[1,0,1]
	v_exp_f32_e32 v82, v28
	v_cvt_pk_fp8_f32 v2, v4, v5 op_sel:[0,0,1]
	v_pk_fma_f32 v[4:5], v[88:89], s[98:99], v[8:9] op_sel_hi:[1,0,1]
	v_exp_f32_e32 v83, v29
	v_max_f32_e32 v4, 0xc1898193, v4
	v_max_f32_e32 v5, 0xc1898193, v5
	v_pk_fma_f32 v[30:31], v[84:85], s[30:31], v[12:13] op_sel_hi:[1,0,1]
	v_exp_f32_e32 v84, v4
	v_exp_f32_e32 v85, v5
	v_pk_fma_f32 v[82:83], v[82:83], s[96:97], s[96:97] op_sel_hi:[1,0,0]
	v_med3_f32 v32, v32, s64, v186
	v_rcp_f32_e32 v82, v82
	v_rcp_f32_e32 v83, v83
	v_med3_f32 v33, v33, s64, v186
	v_pk_fma_f32 v[84:85], v[84:85], s[96:97], s[96:97] op_sel_hi:[1,0,0]
	v_pk_mul_f32 v[28:29], v[28:29], v[32:33]
	v_rcp_f32_e32 v84, v84
	v_rcp_f32_e32 v85, v85
	v_pk_mul_f32 v[28:29], v[28:29], v[82:83]
	v_cvt_pk_fp8_f32 v3, v28, v29
	v_med3_f32 v30, v30, s64, v186
	v_med3_f32 v31, v31, s64, v186
	v_pk_mul_f32 v[4:5], v[4:5], v[30:31]
	v_pk_fma_f32 v[28:29], v[78:79], s[98:99], v[18:19] op_sel_hi:[1,0,1]
	v_pk_mul_f32 v[4:5], v[4:5], v[84:85]
	v_max_f32_e32 v28, 0xc1898193, v28
	v_cvt_pk_fp8_f32 v3, v4, v5 op_sel:[0,0,1]
	v_pk_fma_f32 v[4:5], v[80:81], s[98:99], v[16:17] op_sel_hi:[1,0,1]
	v_max_f32_e32 v29, 0xc1898193, v29
	v_pk_fma_f32 v[32:33], v[74:75], s[30:31], v[22:23] op_sel_hi:[1,0,1]
	v_max_f32_e32 v74, 0xc1898193, v4
	v_max_f32_e32 v75, 0xc1898193, v5
	v_exp_f32_e32 v4, v28
	v_exp_f32_e32 v5, v29
	v_pk_fma_f32 v[30:31], v[76:77], s[30:31], v[20:21] op_sel_hi:[1,0,1]
	v_exp_f32_e32 v76, v74
	v_exp_f32_e32 v77, v75
	v_pk_fma_f32 v[4:5], v[4:5], s[96:97], s[96:97] op_sel_hi:[1,0,0]
	v_med3_f32 v32, v32, s64, v186
	v_rcp_f32_e32 v4, v4
	v_rcp_f32_e32 v5, v5
	v_med3_f32 v33, v33, s64, v186
	v_pk_fma_f32 v[76:77], v[76:77], s[96:97], s[96:97] op_sel_hi:[1,0,0]
	v_pk_mul_f32 v[28:29], v[28:29], v[32:33]
	v_med3_f32 v30, v30, s64, v186
	v_rcp_f32_e32 v76, v76
	v_rcp_f32_e32 v77, v77
	v_pk_mul_f32 v[28:29], v[28:29], v[4:5]
	v_med3_f32 v31, v31, s64, v186
	v_cvt_pk_fp8_f32 v4, v28, v29
	v_pk_mul_f32 v[28:29], v[74:75], v[30:31]
	v_pk_fma_f32 v[30:31], v[70:71], s[98:99], v[10:11] op_sel_hi:[1,0,1]
	v_pk_mul_f32 v[28:29], v[28:29], v[76:77]
	v_max_f32_e32 v30, 0xc1898193, v30
	v_max_f32_e32 v31, 0xc1898193, v31
	v_pk_fma_f32 v[32:33], v[68:69], s[30:31], v[12:13] op_sel_hi:[1,0,1]
	v_exp_f32_e32 v68, v30
	v_cvt_pk_fp8_f32 v4, v28, v29 op_sel:[0,0,1]
	v_pk_fma_f32 v[28:29], v[72:73], s[98:99], v[8:9] op_sel_hi:[1,0,1]
	v_exp_f32_e32 v69, v31
	v_max_f32_e32 v28, 0xc1898193, v28
	v_max_f32_e32 v29, 0xc1898193, v29
	v_exp_f32_e32 v70, v28
	v_exp_f32_e32 v71, v29
	v_pk_fma_f32 v[68:69], v[68:69], s[96:97], s[96:97] op_sel_hi:[1,0,0]
	v_pk_fma_f32 v[66:67], v[66:67], s[30:31], v[14:15] op_sel_hi:[1,0,1]
	v_rcp_f32_e32 v68, v68
	v_rcp_f32_e32 v69, v69
	v_med3_f32 v66, v66, s64, v186
	v_med3_f32 v67, v67, s64, v186
	v_pk_fma_f32 v[70:71], v[70:71], s[96:97], s[96:97] op_sel_hi:[1,0,0]
	v_pk_mul_f32 v[30:31], v[30:31], v[66:67]
	v_rcp_f32_e32 v70, v70
	v_rcp_f32_e32 v71, v71
	v_pk_mul_f32 v[30:31], v[30:31], v[68:69]
	v_cvt_pk_fp8_f32 v5, v30, v31
	v_med3_f32 v32, v32, s64, v186
	v_med3_f32 v33, v33, s64, v186
	v_pk_mul_f32 v[28:29], v[28:29], v[32:33]
	v_pk_fma_f32 v[30:31], v[62:63], s[98:99], v[18:19] op_sel_hi:[1,0,1]
	v_pk_mul_f32 v[28:29], v[28:29], v[70:71]
	v_pk_fma_f32 v[32:33], v[60:61], s[30:31], v[20:21] op_sel_hi:[1,0,1]
	v_cvt_pk_fp8_f32 v5, v28, v29 op_sel:[0,0,1]
	v_pk_fma_f32 v[28:29], v[64:65], s[98:99], v[16:17] op_sel_hi:[1,0,1]
	v_max_f32_e32 v30, 0xc1898193, v30
	v_max_f32_e32 v60, 0xc1898193, v28
	v_max_f32_e32 v31, 0xc1898193, v31
	v_max_f32_e32 v61, 0xc1898193, v29
	v_exp_f32_e32 v28, v30
	v_exp_f32_e32 v62, v60
	v_exp_f32_e32 v63, v61
	v_exp_f32_e32 v29, v31
	v_pk_fma_f32 v[58:59], v[58:59], s[30:31], v[22:23] op_sel_hi:[1,0,1]
	v_med3_f32 v32, v32, s64, v186
	v_med3_f32 v58, v58, s64, v186
	v_pk_fma_f32 v[28:29], v[28:29], s[96:97], s[96:97] op_sel_hi:[1,0,0]
	v_med3_f32 v59, v59, s64, v186
	v_rcp_f32_e32 v28, v28
	v_rcp_f32_e32 v29, v29
	v_pk_fma_f32 v[62:63], v[62:63], s[96:97], s[96:97] op_sel_hi:[1,0,0]
	v_pk_mul_f32 v[30:31], v[30:31], v[58:59]
	v_rcp_f32_e32 v62, v62
	v_rcp_f32_e32 v63, v63
	v_pk_mul_f32 v[30:31], v[30:31], v[28:29]
	v_med3_f32 v33, v33, s64, v186
	v_cvt_pk_fp8_f32 v28, v30, v31
	v_pk_mul_f32 v[30:31], v[60:61], v[32:33]
	v_pk_fma_f32 v[32:33], v[54:55], s[98:99], v[10:11] op_sel_hi:[1,0,1]
	v_pk_mul_f32 v[30:31], v[30:31], v[62:63]
	v_max_f32_e32 v32, 0xc1898193, v32
	v_max_f32_e32 v33, 0xc1898193, v33
	v_exp_f32_e32 v54, v32
	v_cvt_pk_fp8_f32 v28, v30, v31 op_sel:[0,0,1]
	v_pk_fma_f32 v[30:31], v[56:57], s[98:99], v[8:9] op_sel_hi:[1,0,1]
	v_exp_f32_e32 v55, v33
	v_max_f32_e32 v30, 0xc1898193, v30
	v_max_f32_e32 v31, 0xc1898193, v31
	v_exp_f32_e32 v56, v30
	v_exp_f32_e32 v57, v31
	v_pk_fma_f32 v[54:55], v[54:55], s[96:97], s[96:97] op_sel_hi:[1,0,0]
	v_pk_fma_f32 v[50:51], v[50:51], s[30:31], v[14:15] op_sel_hi:[1,0,1]
	v_rcp_f32_e32 v54, v54
	v_rcp_f32_e32 v55, v55
	v_med3_f32 v50, v50, s64, v186
	v_med3_f32 v51, v51, s64, v186
	v_pk_fma_f32 v[56:57], v[56:57], s[96:97], s[96:97] op_sel_hi:[1,0,0]
	v_pk_mul_f32 v[32:33], v[32:33], v[50:51]
	v_rcp_f32_e32 v56, v56
	v_rcp_f32_e32 v57, v57
	v_pk_mul_f32 v[32:33], v[32:33], v[54:55]
	v_pk_fma_f32 v[52:53], v[52:53], s[30:31], v[12:13] op_sel_hi:[1,0,1]
	v_cvt_pk_fp8_f32 v29, v32, v33
	v_med3_f32 v52, v52, s64, v186
	v_med3_f32 v53, v53, s64, v186
	v_pk_mul_f32 v[30:31], v[30:31], v[52:53]
	v_pk_fma_f32 v[16:17], v[48:49], s[98:99], v[16:17] op_sel_hi:[1,0,1]
	v_pk_fma_f32 v[18:19], v[46:47], s[98:99], v[18:19] op_sel_hi:[1,0,1]
	v_pk_mul_f32 v[30:31], v[30:31], v[56:57]
	v_max_f32_e32 v18, 0xc1898193, v18
	v_max_f32_e32 v16, 0xc1898193, v16
	v_cvt_pk_fp8_f32 v29, v30, v31 op_sel:[0,0,1]
	v_max_f32_e32 v19, 0xc1898193, v19
	v_max_f32_e32 v17, 0xc1898193, v17
	v_exp_f32_e32 v30, v18
	v_exp_f32_e32 v32, v16
	v_exp_f32_e32 v33, v17
	v_exp_f32_e32 v31, v19
	v_pk_fma_f32 v[22:23], v[42:43], s[30:31], v[22:23] op_sel_hi:[1,0,1]
	v_pk_fma_f32 v[20:21], v[44:45], s[30:31], v[20:21] op_sel_hi:[1,0,1]
	v_med3_f32 v22, v22, s64, v186
	v_pk_fma_f32 v[30:31], v[30:31], s[96:97], s[96:97] op_sel_hi:[1,0,0]
	v_med3_f32 v23, v23, s64, v186
	v_rcp_f32_e32 v30, v30
	v_rcp_f32_e32 v31, v31
	v_pk_fma_f32 v[32:33], v[32:33], s[96:97], s[96:97] op_sel_hi:[1,0,0]
	v_pk_mul_f32 v[18:19], v[18:19], v[22:23]
	v_rcp_f32_e32 v32, v32
	v_rcp_f32_e32 v33, v33
	v_pk_mul_f32 v[18:19], v[18:19], v[30:31]
	v_cvt_pk_fp8_f32 v30, v18, v19
	v_med3_f32 v20, v20, s64, v186
	v_med3_f32 v21, v21, s64, v186
	v_pk_mul_f32 v[16:17], v[16:17], v[20:21]
	v_pk_fma_f32 v[10:11], v[38:39], s[98:99], v[10:11] op_sel_hi:[1,0,1]
	v_pk_mul_f32 v[16:17], v[16:17], v[32:33]
	v_max_f32_e32 v10, 0xc1898193, v10
	v_max_f32_e32 v11, 0xc1898193, v11
	v_cvt_pk_fp8_f32 v30, v16, v17 op_sel:[0,0,1]
	v_exp_f32_e32 v16, v10
	v_exp_f32_e32 v17, v11
	v_pk_fma_f32 v[8:9], v[40:41], s[98:99], v[8:9] op_sel_hi:[1,0,1]
	v_pk_fma_f32 v[14:15], v[34:35], s[30:31], v[14:15] op_sel_hi:[1,0,1]
	v_max_f32_e32 v8, 0xc1898193, v8
	v_max_f32_e32 v9, 0xc1898193, v9
	v_exp_f32_e32 v18, v8
	v_exp_f32_e32 v19, v9
	v_pk_fma_f32 v[16:17], v[16:17], s[96:97], s[96:97] op_sel_hi:[1,0,0]
	v_med3_f32 v14, v14, s64, v186
	v_rcp_f32_e32 v16, v16
	v_rcp_f32_e32 v17, v17
	v_med3_f32 v15, v15, s64, v186
	v_pk_fma_f32 v[18:19], v[18:19], s[96:97], s[96:97] op_sel_hi:[1,0,0]
	v_pk_mul_f32 v[10:11], v[10:11], v[14:15]
	v_rcp_f32_e32 v18, v18
	v_rcp_f32_e32 v19, v19
	v_pk_mul_f32 v[10:11], v[10:11], v[16:17]
	v_pk_fma_f32 v[12:13], v[36:37], s[30:31], v[12:13] op_sel_hi:[1,0,1]
	v_cvt_pk_fp8_f32 v31, v10, v11
	v_med3_f32 v12, v12, s64, v186
	v_med3_f32 v13, v13, s64, v186
	v_pk_mul_f32 v[8:9], v[8:9], v[12:13]
	v_add_u32_e32 v10, 0x80, v24
	v_pk_mul_f32 v[8:9], v[8:9], v[18:19]
	v_permlane16_swap_b32_e32 v2, v4
	v_cvt_pk_fp8_f32 v31, v8, v9 op_sel:[0,0,1]
	v_or_b32_e32 v8, v10, v25
	v_ashrrev_i32_e32 v9, 31, v8
	v_lshlrev_b64 v[8:9], 10, v[8:9]
	v_lshl_add_u64 v[8:9], s[12:13], 0, v[8:9]
	v_lshl_add_u64 v[8:9], v[8:9], 0, s[38:39]
	v_lshl_add_u64 v[8:9], v[8:9], 0, v[162:163]
	v_permlane16_swap_b32_e32 v3, v5
	v_lshl_add_u64 v[8:9], v[8:9], 0, v[6:7]
	global_store_dwordx4 v[8:9], v[2:5], off
	v_permlane16_swap_b32_e32 v28, v30
	s_nop 0
	v_or_b32_e32 v2, v10, v26
	v_ashrrev_i32_e32 v3, 31, v2
	v_lshlrev_b64 v[2:3], 10, v[2:3]
	v_lshl_add_u64 v[2:3], s[12:13], 0, v[2:3]
	v_lshl_add_u64 v[2:3], v[2:3], 0, s[38:39]
	v_lshl_add_u64 v[2:3], v[2:3], 0, v[162:163]
	v_permlane16_swap_b32_e32 v29, v31
	v_lshl_add_u64 v[2:3], v[2:3], 0, v[6:7]
	s_and_b64 vcc, exec, s[4:5]
	s_mov_b64 s[4:5], -1
	global_store_dwordx4 v[2:3], v[28:31], off
	s_cbranch_vccnz .LBB0_557
	s_andn2_b64 vcc, exec, s[16:17]
	s_cbranch_vccnz .LBB0_569
	s_lshl_b32 s4, s66, 10
	s_and_b32 s4, s4, 0x400
	s_add_i32 s4, s4, 0
	s_ashr_i32 s37, s36, 31
	s_add_i32 s35, s4, 0x24cc0
	s_lshl_b64 s[4:5], s[36:37], 13
	s_add_u32 s37, s14, s4
	s_addc_u32 s38, s15, s5
	s_lshl_b32 s4, s36, 10
	s_lshl_b32 s5, s34, 7
	s_sub_i32 s4, s5, s4
	s_ashr_i32 s5, s4, 31
	s_lshl_b64 s[4:5], s[4:5], 2
	s_add_u32 s4, s37, s4
	s_addc_u32 s5, s38, s5
	s_mov_b32 m0, s35
	s_nop 0
	global_load_lds_dwordx4 v178, s[4:5] offset:0
